# speedup vs baseline: 1.0409x; 1.0409x over previous
_Z7k_attn3PKDF16_S0_PKiS2_PiPKDv8_DF16_PKfS6_S8_Pf:
	s_mov_b32 s75, s2
	s_load_dwordx2 s[12:13], s[0:1], 0x8
	s_load_dwordx2 s[4:5], s[0:1], 0x18
	s_load_dwordx2 s[6:7], s[0:1], 0x28
	s_load_dwordx2 s[16:17], s[0:1], 0x10
	v_lshlrev_b32_e32 v13, 4, v0
	s_mul_i32 s3, s2, 0xc350
	v_or_b32_e32 v1, 0x4000, v13
	s_add_i32 s8, s3, 0xc350
	s_lshl_b32 s20, s2, 2
	s_waitcnt lgkmcnt(0)
	s_add_u32 s4, s4, s20
	s_addc_u32 s5, s5, 0
	s_load_dwordx2 s[18:19], s[4:5], 0x0
	global_load_dwordx4 v[100:103], v13, s[6:7]
	global_load_dwordx4 v[104:107], v1, s[6:7]
	v_or_b32_e32 v1, 0x8000, v13
	s_ashr_i32 s9, s8, 31
	v_or_b32_e32 v2, 0xc000, v13
	global_load_dwordx4 v[108:111], v1, s[6:7]
	global_load_dwordx4 v[112:115], v2, s[6:7]
	v_mov_b32_e32 v116, v13
	s_ashr_i32 s6, s3, 31
	s_lshr_b32 s9, s9, 24
	s_lshr_b32 s6, s6, 24
	s_add_i32 s8, s8, s9
	s_add_i32 s3, s3, s6
	v_lshrrev_b32_e32 v80, 6, v0
	s_ashr_i32 s8, s8, 8
	s_ashr_i32 s66, s3, 8
	s_sub_i32 s33, s8, s66
	v_lshlrev_b32_e32 v1, 1, v80
	v_and_b32_e32 v79, 15, v0
	s_add_i32 s67, s33, -1
	v_or_b32_e32 v11, 1, v1
	v_min_i32_e32 v12, s67, v1
	v_min_i32_e32 v10, s67, v11
	v_cmp_gt_u32_e64 s[38:39], 8, v79
	v_bfe_u32 v28, v0, 4, 2
	v_cmp_eq_u32_e32 vcc, 0, v0
	v_cndmask_b32_e64 v1, v10, v12, s[38:39]
	v_add_u32_e32 v2, s66, v1
	v_ashrrev_i32_e32 v3, 31, v2
	v_lshlrev_b64 v[2:3], 8, v[2:3]
	v_and_b32_e32 v1, 0x70, v13
	v_lshl_add_u64 v[8:9], s[12:13], 0, v[2:3]
	v_lshlrev_b32_e32 v2, 1, v1
	v_lshlrev_b32_e32 v1, 3, v28
	v_mov_b32_e32 v3, 0
	v_and_b32_e32 v22, 8, v1
	v_lshl_add_u64 v[8:9], v[8:9], 0, v[2:3]
	v_lshlrev_b32_e32 v26, 1, v22
	v_mov_b32_e32 v27, v3
	v_lshl_add_u64 v[8:9], v[8:9], 0, v[26:27]
	global_load_dwordx4 v[22:25], v[8:9], off nt
	s_and_saveexec_b64 s[6:7], vcc
	v_mov_b32_e32 v3, 16
	v_mov_b32_e32 v4, 0x26b40
	ds_write_b32 v4, v3
	s_or_b64 exec, exec, s[6:7]
	v_cmp_gt_u32_e32 vcc, 32, v0
	s_and_saveexec_b64 s[6:7], vcc
	v_mov_b32_e32 v3, 0x26d50
	v_lshl_add_u32 v3, v0, 2, v3
	v_mov_b32_e32 v4, 0
	ds_write_b32 v3, v4
	s_or_b64 exec, exec, s[6:7]
	s_movk_i32 s3, 0x100
	v_cmp_gt_u32_e32 vcc, s3, v0
	s_and_saveexec_b64 s[4:5], vcc
	v_mov_b32_e32 v3, 0x1dd00
	v_lshl_add_u32 v3, v0, 2, v3
	v_mov_b32_e32 v4, 0
	ds_write2st64_b32 v3, v4, v4 offset1:4
	s_or_b64 exec, exec, s[4:5]
	s_waitcnt lgkmcnt(0)
	s_add_i32 s76, s18, 3
	s_and_b32 s76, s76, -4
	s_mul_i32 s74, s75, 0x314
	s_add_i32 s76, s76, s74
	s_cmp_gt_i32 s19, s18
	s_cselect_b64 s[6:7], -1, 0
	s_add_i32 s24, s19, -1
	s_cmp_le_i32 s19, s18
	v_add_u32_e32 v3, s18, v0
	v_mov_b32_e32 v13, 0
	v_mov_b32_e32 v15, 0
	s_barrier
	s_cbranch_scc0 .LBB0_50
	v_cndmask_b32_e64 v4, 0, 1, s[6:7]
	v_cmp_ne_u32_e64 s[4:5], 1, v4
	s_andn2_b64 vcc, exec, s[6:7]
	s_cbranch_vccz .LBB0_51

.LBB0_53:
	s_waitcnt lgkmcnt(3)
	v_add_u32_e32 v20, v8, v6
	v_ashrrev_i32_e32 v21, 31, v20
	v_and_b32_e32 v6, 0xffff, v15
	v_subrev_u32_e32 v117, s76, v20
	v_min_u32_e32 v117, 0x400, v117
	v_lshlrev_b32_e32 v117, 2, v117
	v_add_u32_e32 v117, 0x26fd0, v117
	ds_write_b32 v117, v6
	v_lshl_add_u64 v[20:21], v[20:21], 2, s[58:59]
	global_store_dword v[20:21], v6, off
	s_or_b64 exec, exec, s[0:1]
	s_and_saveexec_b64 s[0:1], s[6:7]
	s_cbranch_execz .LBB0_47
.LBB0_54:
	s_waitcnt lgkmcnt(2)
	v_add_u32_e32 v8, v9, v4
	v_ashrrev_i32_e32 v9, 31, v8
	v_and_b32_e32 v4, 0xffff, v13
	v_subrev_u32_e32 v117, s76, v8
	v_min_u32_e32 v117, 0x400, v117
	v_lshlrev_b32_e32 v117, 2, v117
	v_add_u32_e32 v117, 0x26fd0, v117
	ds_write_b32 v117, v4
	v_lshl_add_u64 v[8:9], v[8:9], 2, s[58:59]
	global_store_dword v[8:9], v4, off
	s_or_b64 exec, exec, s[0:1]
	s_and_saveexec_b64 s[0:1], s[8:9]
	s_cbranch_execz .LBB0_48
.LBB0_55:
	s_waitcnt lgkmcnt(1)
	v_add_u32_e32 v6, v18, v7
	v_ashrrev_i32_e32 v7, 31, v6
	v_and_b32_e32 v4, 0xffff, v16
	v_subrev_u32_e32 v117, s76, v6
	v_min_u32_e32 v117, 0x400, v117
	v_lshlrev_b32_e32 v117, 2, v117
	v_add_u32_e32 v117, 0x26fd0, v117
	ds_write_b32 v117, v4
	v_lshl_add_u64 v[6:7], v[6:7], 2, s[58:59]
	global_store_dword v[6:7], v4, off
	s_or_b64 exec, exec, s[0:1]
	s_and_saveexec_b64 s[0:1], s[10:11]
	s_cbranch_execz .LBB0_49
.LBB0_56:
	s_waitcnt lgkmcnt(0)
	v_add_u32_e32 v4, v17, v5
	v_ashrrev_i32_e32 v5, 31, v4
	v_and_b32_e32 v6, 0xffff, v14
	v_subrev_u32_e32 v117, s76, v4
	v_min_u32_e32 v117, 0x400, v117
	v_lshlrev_b32_e32 v117, 2, v117
	v_add_u32_e32 v117, 0x26fd0, v117
	ds_write_b32 v117, v6
	v_lshl_add_u64 v[4:5], v[4:5], 2, s[58:59]
	global_store_dword v[4:5], v6, off
	s_or_b64 exec, exec, s[0:1]
	s_andn2_b64 vcc, exec, s[20:21]
	s_cbranch_vccnz .LBB0_67

.LBB0_87:
	s_or_b64 exec, exec, s[4:5]
	v_readfirstlane_b32 s74, v4
	v_cmp_lt_i32_e64 s[0:1], v79, v99
	v_add_u32_e32 v4, v4, v79
	s_waitcnt vmcnt(0)
	s_and_b64 s[0:1], vcc, s[0:1]
	s_sub_i32 s74, s74, s76
	s_add_i32 s95, s74, 16
	s_cmp_gt_u32 s95, 0x400
	s_cbranch_scc1 .Lent_global
	s_cmp_lg_u64 s[20:21], 0
	s_cbranch_scc1 .Lent_global
	v_subrev_u32_e32 v8, s76, v4
	v_cndmask_b32_e64 v8, 0, v8, s[0:1]
	v_lshlrev_b32_e32 v8, 2, v8
	v_add_u32_e32 v8, 0x26fd0, v8
	ds_read_b32 v4, v8
	s_branch .Lent_done
.Lent_global:
	v_ashrrev_i32_e32 v7, 31, v4
	v_cndmask_b32_e64 v9, 0, v7, s[0:1]
	v_cndmask_b32_e64 v8, 0, v4, s[0:1]
	v_lshl_add_u64 v[8:9], v[8:9], 2, s[58:59]
	global_load_dword v4, v[8:9], off
.Lent_done:
	v_lshrrev_b32_e32 v7, 5, v3
	v_and_b32_e32 v8, 1, v0
	v_cmp_eq_u32_e64 s[4:5], v7, v8
	v_mov_b32_e32 v8, v6
	v_mov_b32_e32 v9, v6
	v_mov_b32_e32 v7, v6
	v_mov_b64_e32 v[12:13], v[8:9]
	v_mov_b64_e32 v[16:17], v[8:9]
	v_mov_b64_e32 v[20:21], v[8:9]
	v_lshlrev_b32_e32 v86, 4, v3
	v_mov_b64_e32 v[10:11], v[6:7]
	v_mov_b64_e32 v[14:15], v[6:7]
	v_mov_b64_e32 v[18:19], v[6:7]
.LBB0_89:
	v_mov_b32_e32 v112, v22
	v_mov_b32_e32 v113, v23
	v_mov_b32_e32 v114, v24
	v_mov_b32_e32 v115, v25
	v_mov_b32_e32 v3, 0
	v_lshlrev_b32_e32 v70, 4, v28
	s_and_saveexec_b64 s[60:61], vcc
	s_cbranch_execz .LBB0_118
	s_mov_b64 s[92:93], s[14:15]
	v_lshl_add_u64 v[22:23], s[12:13], 0, v[2:3]
	s_waitcnt vmcnt(0) lgkmcnt(0)
	v_cndmask_b32_e64 v55, -1, v4, s[0:1]
	s_movk_i32 s0, 0x880
	v_mov_b32_e32 v2, 0x1dd00
	v_mad_u32_u24 v4, v80, s0, v2
	v_lshlrev_b32_e32 v2, 1, v1
	v_mov_b32_e32 v27, v3
	v_mbcnt_hi_u32_b32 v2, -1, v29
	v_lshl_add_u64 v[72:73], v[22:23], 0, v[26:27]
	v_and_b32_e32 v23, 64, v2
	v_xor_b32_e32 v22, 16, v2
	v_add_u32_e32 v23, 64, v23
	v_cmp_lt_i32_e32 vcc, v22, v23
	v_lshlrev_b32_e32 v88, 2, v28
	v_and_b32_e32 v24, 7, v0
	v_cndmask_b32_e32 v22, v2, v22, vcc
	v_lshlrev_b32_e32 v90, 2, v22
	v_xor_b32_e32 v22, 32, v2
	v_cmp_lt_i32_e32 vcc, v22, v23
	s_mov_b32 s24, 0x10000
	v_cndmask_b32_e32 v2, v2, v22, vcc
	v_lshlrev_b32_e32 v91, 2, v2
	v_lshrrev_b32_e32 v2, 2, v79
	v_mul_u32_u24_e32 v22, 0x88, v79
	v_add3_u32 v92, v4, v22, v1
	v_or_b32_e32 v2, v88, v2
	v_lshlrev_b32_e32 v22, 3, v0
	v_mul_u32_u24_e32 v2, 0x88, v2
	v_and_b32_e32 v22, 24, v22
	v_add3_u32 v93, v4, v2, v22
	v_lshlrev_b32_e32 v2, 5, v24
	v_or3_b32 v78, v2, v1, s24
	v_bfe_u32 v2, v0, 1, 2
	v_lshrrev_b32_e32 v89, 3, v79
	v_cmp_eq_u32_e64 s[6:7], 4, v24
	v_cmp_eq_u32_e64 s[8:9], 3, v24
	v_cmp_eq_u32_e64 s[10:11], 2, v24
	v_cmp_eq_u32_e64 s[12:13], 1, v24
	v_cmp_eq_u32_e64 s[14:15], 0, v24
	v_cmp_eq_u32_e64 s[16:17], 7, v24
	v_cmp_eq_u32_e64 s[18:19], 6, v24
	v_cmp_eq_u32_e64 s[20:21], 5, v24
	v_cmp_eq_u32_e64 s[22:23], 0, v2
	v_cmp_eq_u32_e64 s[24:25], 1, v2
	v_cmp_eq_u32_e64 s[26:27], 2, v2
	v_cmp_eq_u32_e64 s[28:29], 3, v2
	s_and_b64 s[22:23], s[22:23], s[4:5]
	s_and_b64 s[24:25], s[24:25], s[4:5]
	s_and_b64 s[26:27], s[26:27], s[4:5]
	s_and_b64 s[28:29], s[28:29], s[4:5]
	v_mov_b32_e32 v71, 0xf149f2ca
	s_mov_b64 s[62:63], 0
	s_mov_b32 s69, 0xf149f2ca
	s_mov_b32 s70, 0xefa18f08
	s_mov_b32 s71, 0x41000000
	s_movk_i32 s72, 0x110
	s_mov_b32 s77, 0x26500
	s_mov_b32 s73, 0x2650c
	s_mov_b32 s80, -1
	s_mov_b32 s81, 0
	s_mov_b32 s82, 0
	s_mov_b32 s83, 0x7fffffff
	s_mov_b64 s[84:85], 0
	v_mov_b32_e32 v100, 0
	v_mov_b32_e32 v4, 0
	v_mov_b32_e32 v103, 0xf149f2ca
	v_mov_b32_e32 v46, v3
	v_mov_b32_e32 v47, v3
	v_mov_b32_e32 v48, v3
	v_mov_b32_e32 v49, v3
	v_mov_b32_e32 v50, v3
	v_mov_b32_e32 v51, v3
	v_mov_b32_e32 v52, v3
	v_mov_b32_e32 v53, v3
	v_mov_b32_e32 v38, v3
	v_mov_b32_e32 v39, v3
	v_mov_b32_e32 v40, v3
	v_mov_b32_e32 v41, v3
	v_mov_b32_e32 v42, v3
	v_mov_b32_e32 v43, v3
	v_mov_b32_e32 v44, v3
	v_mov_b32_e32 v45, v3
	v_mov_b32_e32 v30, v3
	v_mov_b32_e32 v31, v3
	v_mov_b32_e32 v32, v3
	v_mov_b32_e32 v33, v3
	v_mov_b32_e32 v34, v3
	v_mov_b32_e32 v35, v3
	v_mov_b32_e32 v36, v3
	v_mov_b32_e32 v37, v3
	v_mov_b32_e32 v22, v3
	v_mov_b32_e32 v23, v3
	v_mov_b32_e32 v24, v3
	v_mov_b32_e32 v25, v3
	v_mov_b32_e32 v26, v3
	v_mov_b32_e32 v28, v3
	v_mov_b32_e32 v29, v3
	v_readfirstlane_b32 s86, v80
	s_mov_b32 s87, 0
	v_readfirstlane_b32 s88, v99
	v_readfirstlane_b32 s89, v5
	v_readfirstlane_b32 s96, v54
	v_readfirstlane_b32 s97, v84
	v_readfirstlane_b32 s98, v85
	v_readfirstlane_b32 s99, v81
	v_readfirstlane_b32 s100, v83
	v_readfirstlane_b32 s101, v82
	v_mov_b32_e32 v84, v82
	s_cmp_ge_i32 s96, s68
	s_cselect_b32 s100, 0, s100
	s_branch .LBB0_95

	.amdhsa_kernel _Z7k_attn3PKDF16_S0_PKiS2_PiPKDv8_DF16_PKfS6_S8_Pf
		.amdhsa_group_segment_fixed_size 163796
		.amdhsa_private_segment_fixed_size 0
		.amdhsa_kernarg_size 80
		.amdhsa_user_sgpr_count 2
		.amdhsa_user_sgpr_dispatch_ptr 0
		.amdhsa_user_sgpr_queue_ptr 0
		.amdhsa_user_sgpr_kernarg_segment_ptr 1
		.amdhsa_user_sgpr_dispatch_id 0
		.amdhsa_user_sgpr_kernarg_preload_length 0
		.amdhsa_user_sgpr_kernarg_preload_offset 0
		.amdhsa_user_sgpr_private_segment_size 0
		.amdhsa_uses_dynamic_stack 0
		.amdhsa_enable_private_segment 0
		.amdhsa_system_sgpr_workgroup_id_x 1
		.amdhsa_system_sgpr_workgroup_id_y 0
		.amdhsa_system_sgpr_workgroup_id_z 0
		.amdhsa_system_sgpr_workgroup_info 0
		.amdhsa_system_vgpr_workitem_id 0
		.amdhsa_next_free_vgpr 128
		.amdhsa_next_free_sgpr 102
		.amdhsa_accum_offset 128
		.amdhsa_reserve_vcc 1
		.amdhsa_float_round_mode_32 0
		.amdhsa_float_round_mode_16_64 0
		.amdhsa_float_denorm_mode_32 3
		.amdhsa_float_denorm_mode_16_64 3
		.amdhsa_dx10_clamp 1
		.amdhsa_ieee_mode 1
		.amdhsa_fp16_overflow 0
		.amdhsa_tg_split 0
		.amdhsa_exception_fp_ieee_invalid_op 0
		.amdhsa_exception_fp_denorm_src 0
		.amdhsa_exception_fp_ieee_div_zero 0
		.amdhsa_exception_fp_ieee_overflow 0
		.amdhsa_exception_fp_ieee_underflow 0
		.amdhsa_exception_fp_ieee_inexact 0
		.amdhsa_exception_int_div_zero 0
	.end_amdhsa_kernel

amdhsa.kernels:
  - .agpr_count:     0
    .args:
      - .actual_access:  read_only
        .address_space:  global
        .offset:         0
        .size:           8
        .value_kind:     global_buffer
      - .actual_access:  read_only
        .address_space:  global
        .offset:         8
        .size:           8
        .value_kind:     global_buffer
      - .actual_access:  read_only
        .address_space:  global
        .offset:         16
        .size:           8
        .value_kind:     global_buffer
      - .actual_access:  read_only
        .address_space:  global
        .offset:         24
        .size:           8
        .value_kind:     global_buffer
      - .address_space:  global
        .offset:         32
        .size:           8
        .value_kind:     global_buffer
      - .actual_access:  read_only
        .address_space:  global
        .offset:         40
        .size:           8
        .value_kind:     global_buffer
      - .actual_access:  read_only
        .address_space:  global
        .offset:         48
        .size:           8
        .value_kind:     global_buffer
      - .actual_access:  read_only
        .address_space:  global
        .offset:         56
        .size:           8
        .value_kind:     global_buffer
      - .actual_access:  read_only
        .address_space:  global
        .offset:         64
        .size:           8
        .value_kind:     global_buffer
      - .actual_access:  write_only
        .address_space:  global
        .offset:         72
        .size:           8
        .value_kind:     global_buffer
    .group_segment_fixed_size: 163796
    .kernarg_segment_align: 8
    .kernarg_segment_size: 80
    .language:       OpenCL C
    .language_version:
      - 2
      - 0
    .max_flat_workgroup_size: 1024
    .name:           _Z7k_attn3PKDF16_S0_PKiS2_PiPKDv8_DF16_PKfS6_S8_Pf
    .private_segment_fixed_size: 0
    .sgpr_count:     79
    .sgpr_spill_count: 0
    .symbol:         _Z7k_attn3PKDF16_S0_PKiS2_PiPKDv8_DF16_PKfS6_S8_Pf.kd
    .uniform_work_group_size: 1
    .uses_dynamic_stack: false
    .vgpr_count:     128
    .vgpr_spill_count: 0
    .wavefront_size: 64
  - .agpr_count:     0
    .args:
      - .actual_access:  read_only
        .address_space:  global
        .offset:         0
        .size:           8
        .value_kind:     global_buffer
      - .actual_access:  write_only
        .address_space:  global
        .offset:         8
        .size:           8
        .value_kind:     global_buffer
      - .actual_access:  read_only
        .address_space:  global
        .offset:         16
        .size:           8
        .value_kind:     global_buffer
      - .actual_access:  read_only
        .address_space:  global
        .offset:         24
        .size:           8
        .value_kind:     global_buffer
      - .actual_access:  read_only
        .address_space:  global
        .offset:         32
        .size:           8
        .value_kind:     global_buffer
      - .actual_access:  read_only
        .address_space:  global
        .offset:         40
        .size:           8
        .value_kind:     global_buffer
      - .actual_access:  read_only
        .address_space:  global
        .offset:         48
        .size:           8
        .value_kind:     global_buffer
      - .actual_access:  read_only
        .address_space:  global
        .offset:         56
        .size:           8
        .value_kind:     global_buffer
      - .actual_access:  read_only
        .address_space:  global
        .offset:         64
        .size:           8
        .value_kind:     global_buffer
      - .actual_access:  write_only
        .address_space:  global
        .offset:         72
        .size:           8
        .value_kind:     global_buffer
      - .actual_access:  write_only
        .address_space:  global
        .offset:         80
        .size:           8
        .value_kind:     global_buffer
      - .actual_access:  write_only
        .address_space:  global
        .offset:         88
        .size:           8
        .value_kind:     global_buffer
      - .actual_access:  write_only
        .address_space:  global
        .offset:         96
        .size:           8
        .value_kind:     global_buffer
    .group_segment_fixed_size: 1024
    .kernarg_segment_align: 8
    .kernarg_segment_size: 104
    .language:       OpenCL C
    .language_version:
      - 2
      - 0
    .max_flat_workgroup_size: 512
    .name:           _Z4k_l1PK15HIP_vector_typeIiLj4EEPiPKfS5_S5_S5_S5_S5_S5_PDF16_PfS6_S6_
    .private_segment_fixed_size: 0
    .sgpr_count:     22
    .sgpr_spill_count: 0
    .symbol:         _Z4k_l1PK15HIP_vector_typeIiLj4EEPiPKfS5_S5_S5_S5_S5_S5_PDF16_PfS6_S6_.kd
    .uniform_work_group_size: 1
    .uses_dynamic_stack: false
    .vgpr_count:     24
    .vgpr_spill_count: 0
    .wavefront_size: 64
  - .agpr_count:     0
    .args:
      - .actual_access:  read_only
        .address_space:  global
        .offset:         0
        .size:           8
        .value_kind:     global_buffer
      - .actual_access:  read_only
        .address_space:  global
        .offset:         8
        .size:           8
        .value_kind:     global_buffer
      - .actual_access:  read_only
        .address_space:  global
        .offset:         16
        .size:           8
        .value_kind:     global_buffer
      - .actual_access:  write_only
        .address_space:  global
        .offset:         24
        .size:           8
        .value_kind:     global_buffer
      - .actual_access:  write_only
        .address_space:  global
        .offset:         32
        .size:           8
        .value_kind:     global_buffer
      - .actual_access:  read_only
        .address_space:  global
        .offset:         40
        .size:           8
        .value_kind:     global_buffer
      - .actual_access:  read_only
        .address_space:  global
        .offset:         48
        .size:           8
        .value_kind:     global_buffer
      - .actual_access:  read_only
        .address_space:  global
        .offset:         56
        .size:           8
        .value_kind:     global_buffer
      - .actual_access:  write_only
        .address_space:  global
        .offset:         64
        .size:           8
        .value_kind:     global_buffer
      - .actual_access:  write_only
        .address_space:  global
        .offset:         72
        .size:           8
        .value_kind:     global_buffer
    .group_segment_fixed_size: 53248
    .kernarg_segment_align: 8
    .kernarg_segment_size: 80
    .language:       OpenCL C
    .language_version:
      - 2
      - 0
    .max_flat_workgroup_size: 512
    .name:           _Z4k_l2PK15HIP_vector_typeIiLj4EES2_PKiPiS5_PKfPKDv8_DF16_S7_PDF16_SB_
    .private_segment_fixed_size: 0
    .sgpr_count:     34
    .sgpr_spill_count: 0
    .symbol:         _Z4k_l2PK15HIP_vector_typeIiLj4EES2_PKiPiS5_PKfPKDv8_DF16_S7_PDF16_SB_.kd
    .uniform_work_group_size: 1
    .uses_dynamic_stack: false
    .vgpr_count:     126
    .vgpr_spill_count: 0
    .wavefront_size: 64
